# grid barrier: the second-to-last local arrival of an XCD starts the L2 write-back early (leader's write-back then only has the tail)
# baseline (speedup 1.0000x reference)
.LBB0_190:
	v_readlane_b32 s4, v254, 43
	s_lshl_b32 s4, s4, 8
	v_readlane_b32 s6, v254, 40
	v_readlane_b32 s7, v254, 41
	s_add_u32 s4, s6, s4
	s_addc_u32 s5, s7, 0
	v_mov_b32_e32 v2, 0x1000
	v_mov_b32_e32 v4, 1
	global_atomic_add v4, v2, v4, s[4:5] offset:1024 sc0
	v_cvt_f32_u32_e32 v2, v3
	v_sub_u32_e32 v5, 0, v3
	v_rcp_iflag_f32_e32 v2, v2
	s_nop 0
	v_mul_f32_e32 v2, 0x4f7ffffe, v2
	v_cvt_u32_f32_e32 v2, v2
	v_mul_lo_u32 v5, v5, v2
	v_mul_hi_u32 v5, v2, v5
	v_add_u32_e32 v2, v2, v5
	s_waitcnt vmcnt(0)
	v_mul_hi_u32 v2, v4, v2
	v_mul_lo_u32 v5, v2, v3
	v_sub_u32_e32 v5, v4, v5
	v_add_u32_e32 v6, 1, v2
	v_cmp_ge_u32_e32 vcc, v5, v3
	v_add_u32_e32 v4, 1, v4
	s_nop 0
	v_cndmask_b32_e32 v2, v2, v6, vcc
	v_sub_u32_e32 v6, v5, v3
	v_cndmask_b32_e32 v5, v5, v6, vcc
	v_add_u32_e32 v6, 1, v2
	v_cmp_ge_u32_e32 vcc, v5, v3
	s_nop 1
	v_cndmask_b32_e32 v2, v2, v6, vcc
	v_mul_lo_u32 v5, v3, v2
	v_add_u32_e32 v3, v5, v3
	v_cmp_ne_u32_e32 vcc, v4, v3
	s_cbranch_vccz .Lxb0_lead
	v_sub_u32_e32 v6, v3, v4
	v_cmp_eq_u32_e32 vcc, 1, v6
	s_cbranch_vccz .Lxb0_poll
	buffer_wbl2 sc1

.LBB0_248:
	v_readlane_b32 s2, v254, 43
	s_lshl_b32 s2, s2, 8
	v_readlane_b32 s4, v254, 40
	v_readlane_b32 s5, v254, 41
	s_add_u32 s2, s4, s2
	s_addc_u32 s3, s5, 0
	v_mov_b32_e32 v2, 0x1000
	v_mov_b32_e32 v4, 1
	global_atomic_add v4, v2, v4, s[2:3] offset:1024 sc0
	v_cvt_f32_u32_e32 v2, v3
	v_sub_u32_e32 v5, 0, v3
	v_rcp_iflag_f32_e32 v2, v2
	s_nop 0
	v_mul_f32_e32 v2, 0x4f7ffffe, v2
	v_cvt_u32_f32_e32 v2, v2
	v_mul_lo_u32 v5, v5, v2
	v_mul_hi_u32 v5, v2, v5
	v_add_u32_e32 v2, v2, v5
	s_waitcnt vmcnt(0)
	v_mul_hi_u32 v2, v4, v2
	v_mul_lo_u32 v5, v2, v3
	v_sub_u32_e32 v5, v4, v5
	v_add_u32_e32 v6, 1, v2
	v_cmp_ge_u32_e32 vcc, v5, v3
	v_add_u32_e32 v4, 1, v4
	s_nop 0
	v_cndmask_b32_e32 v2, v2, v6, vcc
	v_sub_u32_e32 v6, v5, v3
	v_cndmask_b32_e32 v5, v5, v6, vcc
	v_add_u32_e32 v6, 1, v2
	v_cmp_ge_u32_e32 vcc, v5, v3
	s_nop 1
	v_cndmask_b32_e32 v2, v2, v6, vcc
	v_mul_lo_u32 v5, v3, v2
	v_add_u32_e32 v3, v5, v3
	v_cmp_ne_u32_e32 vcc, v4, v3
	s_cbranch_vccz .Lxb1_lead
	v_sub_u32_e32 v6, v3, v4
	v_cmp_eq_u32_e32 vcc, 1, v6
	s_cbranch_vccz .Lxb1_poll
	buffer_wbl2 sc1

.LBB0_3782:
	v_readlane_b32 s4, v254, 43
	s_lshl_b32 s4, s4, 8
	v_readlane_b32 s8, v254, 40
	v_readlane_b32 s9, v254, 41
	s_add_u32 s4, s8, s4
	s_addc_u32 s5, s9, 0
	v_mov_b32_e32 v2, 0x1000
	v_mov_b32_e32 v4, 1
	global_atomic_add v4, v2, v4, s[4:5] offset:1024 sc0
	v_cvt_f32_u32_e32 v2, v3
	v_sub_u32_e32 v5, 0, v3
	v_rcp_iflag_f32_e32 v2, v2
	s_nop 0
	v_mul_f32_e32 v2, 0x4f7ffffe, v2
	v_cvt_u32_f32_e32 v2, v2
	v_mul_lo_u32 v5, v5, v2
	v_mul_hi_u32 v5, v2, v5
	v_add_u32_e32 v2, v2, v5
	s_waitcnt vmcnt(0)
	v_mul_hi_u32 v2, v4, v2
	v_mul_lo_u32 v5, v2, v3
	v_sub_u32_e32 v5, v4, v5
	v_add_u32_e32 v6, 1, v2
	v_cmp_ge_u32_e32 vcc, v5, v3
	v_add_u32_e32 v4, 1, v4
	s_nop 0
	v_cndmask_b32_e32 v2, v2, v6, vcc
	v_sub_u32_e32 v6, v5, v3
	v_cndmask_b32_e32 v5, v5, v6, vcc
	v_add_u32_e32 v6, 1, v2
	v_cmp_ge_u32_e32 vcc, v5, v3
	s_nop 1
	v_cndmask_b32_e32 v2, v2, v6, vcc
	v_mul_lo_u32 v5, v3, v2
	v_add_u32_e32 v3, v5, v3
	v_cmp_ne_u32_e32 vcc, v4, v3
	s_cbranch_vccz .Lxb13_lead
	v_sub_u32_e32 v6, v3, v4
	v_cmp_eq_u32_e32 vcc, 1, v6
	s_cbranch_vccz .Lxb13_poll
	buffer_wbl2 sc1
